# grid barrier: the cache invalidate is issued by wave 1 in parallel with wave 0's arrive/poll protocol
# baseline (speedup 1.0000x reference)
.Lgb_poll_0:
.Lgb_spin_0:
	global_load_dword v11, v6, s[100:101] sc1
	v_add_u32_e32 v10, 1, v10
	s_waitcnt vmcnt(0)
	v_cmp_ge_u32_e32 vcc, v11, v9
	s_cbranch_vccnz .Lgb_done_0
	v_cmp_gt_u32_e32 vcc, 0x80000, v10
	s_sleep 1
	s_cbranch_vccnz .Lgb_spin_0
.Lgb_done_0:
	s_waitcnt lgkmcnt(0)
	s_branch .LBB0_283
.Lgb_other_0:
	s_cmp_lg_u32 s92, 1
	s_cbranch_scc1 .LBB0_283
	s_mov_b64 exec, 1
	buffer_inv sc1
	s_waitcnt vmcnt(0)

.Lgb_poll_3:
.Lgb_spin_3:
	global_load_dword v17, v12, s[100:101] sc1
	v_add_u32_e32 v16, 1, v16
	s_waitcnt vmcnt(0)
	v_cmp_ge_u32_e32 vcc, v17, v15
	s_cbranch_vccnz .Lgb_done_3
	v_cmp_gt_u32_e32 vcc, 0x80000, v16
	s_sleep 1
	s_cbranch_vccnz .Lgb_spin_3

.Lgb_poll_10:
.Lgb_spin_10:
	global_load_dword v12, v7, s[100:101] sc1
	v_add_u32_e32 v11, 1, v11
	s_waitcnt vmcnt(0)
	v_cmp_ge_u32_e32 vcc, v12, v10
	s_cbranch_vccnz .Lgb_done_10
	v_cmp_gt_u32_e32 vcc, 0x80000, v11
	s_sleep 1
	s_cbranch_vccnz .Lgb_spin_10
